# attn: key-tile rotation (2qb+21head)&31
# baseline (speedup 1.0000x reference)
.Lp_top:
	s_lshl_b32 s6, s21, 20
	s_add_u32 s4, s4, s6
	s_addc_u32 s5, s5, 0
	v_lshlrev_b32_e32 v54, 4, v0
	v_mov_b32_e32 v55, v63
	s_lshl_b32 s3, s3, 1
	s_mul_i32 s20, s21, 21
	v_lshl_add_u64 v[4:5], s[4:5], 0, v[54:55]
	s_mov_b64 s[4:5], 0x1000000
	s_add_i32 s20, s20, s3
	v_lshl_add_u64 v[170:171], v[4:5], 0, s[4:5]
	s_and_b32 s22, s20, 31
	s_lshl_b32 s4, s20, 12
	s_lshl_b32 s12, s22, 13
	s_add_i32 s5, s4, 0x1000
	v_lshl_add_u64 v[58:59], v[170:171], 0, s[12:13]
	s_mov_b32 s3, 0x80000
	s_and_b32 s5, s5, 0x1f000
	v_add_co_u32_e32 v16, vcc, s3, v58
	s_lshl_b32 s12, s5, 1
	s_nop 0
	v_addc_co_u32_e32 v17, vcc, 0, v59, vcc
	v_lshl_add_u64 v[56:57], v[170:171], 0, s[12:13]
	global_load_dwordx4 v[4:7], v[58:59], off
	global_load_dwordx4 v[8:11], v[56:57], off
	global_load_dwordx4 v[12:15], v[16:17], off
	v_add_co_u32_e32 v16, vcc, s3, v56
	v_lshrrev_b32_e32 v184, 8, v0
	s_nop 0
	v_addc_co_u32_e32 v17, vcc, 0, v57, vcc
	global_load_dwordx4 v[16:19], v[16:17], off
	v_and_b32_e32 v20, 19, v0
	v_lshlrev_b32_e32 v21, 1, v0
	v_and_b32_e32 v2, 4, v2
	v_and_or_b32 v20, v21, 8, v20
	v_lshlrev_b32_e32 v101, 5, v184
	s_addk_i32 s4, 0x2000
	v_or3_b32 v2, v20, v2, v101
	s_and_b32 s4, s4, 0x1f000
	v_mul_u32_u24_e32 v2, 0x48, v2
	s_lshl_b32 s12, s4, 1
	v_lshlrev_b32_e32 v3, 3, v0
	v_lshlrev_b32_e32 v100, 1, v99
	v_lshlrev_b32_e32 v2, 1, v2
	v_lshl_add_u64 v[60:61], v[170:171], 0, s[12:13]
	v_and_b32_e32 v3, 56, v3
	v_add3_u32 v186, 0, v2, v100
	v_add_co_u32_e32 v2, vcc, s3, v60
	v_lshlrev_b32_e32 v68, 1, v3
	s_nop 0
	v_addc_co_u32_e32 v3, vcc, 0, v61, vcc
	global_load_dwordx4 v[162:165], v[60:61], off
	global_load_dwordx4 v[166:169], v[2:3], off
	v_lshrrev_b32_e32 v82, 3, v0
	v_mul_u32_u24_e32 v22, 0x48, v82
	v_lshlrev_b32_e32 v21, 1, v22
	v_add3_u32 v185, 0, v21, v68
	s_mov_b64 s[24:25], 0x80000
	s_add_i32 s17, s20, 3
	s_add_i32 s18, s20, 4
	v_mov_b32_e32 v62, v63
	v_lshrrev_b32_e32 v55, 6, v0
	v_mov_b32_e32 v83, 0
	v_mov_b32_e32 v84, 0
	v_lshl_add_u64 v[70:71], v[58:59], 0, s[24:25]
	v_lshl_add_u64 v[66:67], v[56:57], 0, s[24:25]
	v_lshl_add_u64 v[64:65], v[60:61], 0, s[24:25]
	s_waitcnt vmcnt(5)
	ds_write_b128 v185, v[4:7]
	s_waitcnt vmcnt(3)
	ds_write_b128 v185, v[12:15] offset:9216
	ds_write_b128 v185, v[8:11] offset:18432
	s_waitcnt vmcnt(2)
	ds_write_b128 v185, v[16:19] offset:27648
	s_waitcnt lgkmcnt(0)
	s_barrier
	ds_read_b128 v[2:5], v186
	ds_read_b128 v[38:41], v186 offset:32
	s_waitcnt lgkmcnt(1)
	v_mfma_f32_32x32x16_f16 v[2:17], v[2:5], v[114:117], 0
	ds_read_b128 v[18:21], v186 offset:9216
	ds_read_b128 v[46:49], v186 offset:9248
	s_waitcnt lgkmcnt(1)
	v_mfma_f32_32x32x16_f16 v[18:33], v[18:21], v[130:133], 0
	v_mfma_f32_32x32x16_f16 v[2:17], v[38:41], v[118:121], v[2:17]
	s_waitcnt lgkmcnt(0)
	v_mfma_f32_32x32x16_f16 v[18:33], v[46:49], v[134:137], v[18:33]
	ds_read_b128 v[38:41], v186 offset:64
	ds_read_b128 v[46:49], v186 offset:96
	s_waitcnt lgkmcnt(1)
	v_mfma_f32_32x32x16_f16 v[2:17], v[38:41], v[122:125], v[2:17]
	ds_read_b128 v[38:41], v186 offset:9280
	ds_read_b128 v[50:53], v186 offset:9312
	s_load_dwordx4 s[4:7], s[0:1], 0x38
	s_load_dwordx2 s[14:15], s[0:1], 0x8
	s_mov_b32 s0, -2
	s_mov_b32 s1, 0x3f800000
	s_waitcnt lgkmcnt(0)
	s_barrier
	v_mfma_f32_32x32x16_f16 v[18:33], v[38:41], v[138:141], v[18:33]
	v_mfma_f32_32x32x16_f16 v[2:17], v[46:49], v[126:129], v[2:17]
	v_mfma_f32_32x32x16_f16 v[18:33], v[50:53], v[142:145], v[18:33]
	s_lshl_b32 s12, s17, 13
	s_and_b32 s12, s12, 0x3e000
	s_add_u32 s28, s12, s3
	s_mov_b32 s29, 0
	v_lshl_add_u64 v[176:177], v[170:171], 0, s[12:13]
	global_load_dwordx4 v[50:53], v[176:177], off
	v_lshl_add_u64 v[176:177], v[170:171], 0, s[28:29]
	global_load_dwordx4 v[94:97], v[176:177], off
	s_nop 7
	s_cmp_eq_u32 s37, 1
	s_cbranch_scc0 .Lf_A
	v_mov_b32_e32 v83, 0xf149f2ca
	v_mov_b32_e32 v84, 0xf149f2ca
	s_branch .Ls_A

.Ll1_cont:
	ds_bpermute_b32 v2, v69, v84
	ds_bpermute_b32 v5, v69, v83
	v_max_f32_e32 v4, v84, v84
	v_max_f32_e32 v7, v83, v83
	ds_bpermute_b32 v3, v69, v63
	s_waitcnt lgkmcnt(2)
	v_max_f32_e32 v6, v2, v2
	v_max_f32_e32 v4, v4, v6
	v_sub_f32_e32 v6, v84, v4
	v_exp_f32_e32 v9, v6
	s_waitcnt lgkmcnt(1)
	v_max_f32_e32 v6, v5, v5
	v_sub_f32_e32 v2, v2, v4
	v_max_f32_e32 v6, v7, v6
	v_exp_f32_e32 v11, v2
	ds_bpermute_b32 v2, v69, v62
	v_sub_f32_e32 v5, v5, v6
	v_sub_f32_e32 v7, v83, v6
	v_exp_f32_e32 v10, v5
	v_exp_f32_e32 v8, v7
	v_cmp_gt_u32_e32 vcc, 32, v98
	s_waitcnt lgkmcnt(0)
	v_pk_mul_f32 v[2:3], v[10:11], v[2:3]
	s_nop 0
	v_pk_fma_f32 v[8:9], v[62:63], v[8:9], v[2:3]
	v_lshlrev_b32_e32 v2, 7, v184
	v_or3_b32 v10, v183, v2, v1
	s_and_saveexec_b64 s[0:1], vcc
	v_lshl_add_u32 v2, v10, 4, 0
	v_add_u32_e32 v2, 0x21000, v2
	v_mov_b32_e32 v5, v9
	v_mov_b32_e32 v7, v8
	ds_write_b128 v2, v[4:7]
	s_or_b64 exec, exec, s[0:1]
	s_lshl_b32 s12, s21, 7
	s_mov_b32 s3, 0
	v_or_b32_e32 v2, s12, v82
	s_lshl_b32 s13, s21, 11
	s_add_i32 s23, 0, 0x12000
	v_lshlrev_b32_e32 v2, 12, v2
	v_mov_b32_e32 v3, 0
	s_add_i32 s13, s13, s16
	s_lshl_b64 s[0:1], s[2:3], 13
	v_lshl_add_u64 v[12:13], s[14:15], 0, v[2:3]
	v_mov_b32_e32 v69, v3
	s_add_u32 s0, s10, s0
	v_lshl_add_u64 v[172:173], v[12:13], 0, v[68:69]
	s_addc_u32 s1, s11, s1
	s_lshl_b32 s10, s22, 7
	s_mov_b32 s11, s3
	s_waitcnt vmcnt(1)
	v_lshl_add_u64 v[36:37], v[172:173], 0, s[10:11]
	s_mov_b32 s10, 0x40000
	v_add_co_u32_e32 v38, vcc, s10, v36
	s_waitcnt lgkmcnt(0)
	s_barrier
	global_load_dwordx4 v[12:15], v[58:59], off
	global_load_dwordx4 v[16:19], v[70:71], off
	v_addc_co_u32_e32 v39, vcc, 0, v37, vcc
	global_load_dwordx4 v[20:23], v[56:57], off
	global_load_dwordx4 v[24:27], v[66:67], off
	global_load_dwordx4 v[28:31], v[36:37], off
	global_load_dwordx4 v[32:35], v[38:39], off
	v_add_f32_e32 v2, v78, v80
	s_movk_i32 s11, 0x1200
	v_add_f32_e32 v5, v79, v81
	s_mov_b32 s14, 0x3fb8aa3b
	v_lshlrev_b32_e32 v10, 4, v10
	v_mov_b32_e32 v36, s23
	v_mul_f32_e32 v37, 0x3fb8aa3b, v2
	v_mul_f32_e32 v38, 0x3fb8aa3b, v5
	v_xor_b32_e32 v10, 0x800, v10
	v_mad_u32_u24 v40, v55, s11, v36
	v_fma_f32 v36, v2, s14, -v37
	v_rndne_f32_e32 v39, v37
	v_fma_f32 v41, v5, s14, -v38
	s_waitcnt vmcnt(6)
	v_rndne_f32_e32 v42, v38
	v_add_u32_e32 v10, 0, v10
	v_fmac_f32_e32 v36, 0x32a5705f, v2
	v_sub_f32_e32 v37, v37, v39
	v_fmac_f32_e32 v41, 0x32a5705f, v5
	v_sub_f32_e32 v38, v38, v42
	v_add_u32_e32 v10, 0x21000, v10
	v_add_f32_e32 v44, v37, v36
	global_load_dwordx4 v[146:149], v[60:61], off
	global_load_dwordx4 v[150:153], v[64:65], off
	v_cvt_i32_f32_e32 v43, v39
	v_add_f32_e32 v41, v38, v41
	ds_read_b128 v[36:39], v10
	v_exp_f32_e32 v10, v44
	v_cvt_i32_f32_e32 v42, v42
	v_exp_f32_e32 v41, v41
	s_mov_b32 s21, 0xc2ce8ed0
	s_lshl_b32 s11, s20, 6
	s_add_i32 s14, s11, 64
	v_ldexp_f32 v10, v10, v43
	v_cmp_ngt_f32_e32 vcc, s21, v2
	s_mov_b32 s22, 0x42b17218
	s_and_b32 s14, s14, 0x7c0
	v_ldexp_f32 v41, v41, v42
	v_cndmask_b32_e32 v10, 0, v10, vcc
	v_cmp_ngt_f32_e32 vcc, s21, v5
	v_mov_b32_e32 v7, 0x7f800000
	v_max_f32_e32 v11, v4, v4
	s_mov_b32 s15, s3
	s_lshl_b32 s14, s14, 1
	s_waitcnt lgkmcnt(0)
	v_max_f32_e32 v42, v36, v36
	v_cndmask_b32_e32 v41, 0, v41, vcc
	v_cmp_nlt_f32_e32 vcc, s22, v2
	v_max_f32_e32 v187, v11, v42
	v_mov_b32_e32 v55, v3
	v_cndmask_b32_e32 v2, v7, v10, vcc
	v_cmp_nlt_f32_e32 vcc, s22, v5
	v_lshl_add_u64 v[10:11], v[172:173], 0, s[14:15]
	v_lshl_add_u64 v[178:179], s[0:1], 0, v[54:55]
	v_cndmask_b32_e32 v5, v7, v41, vcc
	v_sub_f32_e32 v2, v2, v5
	v_add_f32_e32 v41, 0x3e4ccccd, v2
	v_sub_f32_e32 v2, v4, v187
	v_max_f32_e32 v4, v6, v6
	s_and_b32 s1, s2, 7
	s_mulk_i32 s1, 0xa80
	s_mulk_i32 s19, 0x540
	s_add_i32 s0, s20, 2
	s_waitcnt vmcnt(7)
	ds_write_b128 v185, v[12:15]
	s_waitcnt vmcnt(6)
	ds_write_b128 v185, v[16:19] offset:9216
	s_waitcnt vmcnt(5)
	ds_write_b128 v185, v[20:23] offset:18432
	s_waitcnt vmcnt(4)
	ds_write_b128 v185, v[24:27] offset:27648
	s_waitcnt vmcnt(3)
	ds_write_b128 v185, v[28:31] offset:36864
	s_waitcnt vmcnt(2)
	ds_write_b128 v185, v[32:35] offset:46080
	v_add_co_u32_e32 v12, vcc, s10, v10
	v_exp_f32_e32 v23, v2
	s_nop 0
	v_addc_co_u32_e32 v13, vcc, 0, v11, vcc
	global_load_dwordx4 v[154:157], v[10:11], off
	global_load_dwordx4 v[158:161], v[12:13], off
	s_waitcnt lgkmcnt(0)
	s_barrier
	ds_read_b128 v[10:13], v186
	v_sub_f32_e32 v2, v36, v187
	v_exp_f32_e32 v25, v2
	v_max_f32_e32 v2, v38, v38
	v_max_f32_e32 v188, v4, v2
	v_sub_f32_e32 v2, v6, v188
	v_exp_f32_e32 v22, v2
	v_sub_f32_e32 v2, v38, v188
	v_exp_f32_e32 v24, v2
	ds_read_b128 v[14:17], v186 offset:9216
	ds_read_b128 v[18:21], v186 offset:32
	s_waitcnt lgkmcnt(2)
	v_mfma_f32_32x32x16_f16 v[66:81], v[10:13], v[114:117], 0
	v_mov_b32_e32 v36, v39
	v_mul_f32_e64 v10, v36, v24
	v_mul_f32_e64 v11, v37, v25
	ds_read_b128 v[4:7], v186 offset:9248
	s_add_i32 s1, s1, s19
	s_mov_b32 s14, 0x30000
	s_mov_b32 s15, 0x80000
	s_mov_b32 s19, 0
	s_waitcnt lgkmcnt(2)
	v_mfma_f32_32x32x16_f16 v[82:97], v[14:17], v[130:133], 0
	v_fma_f32 v16, v8, v22, v10
	v_fma_f32 v17, v9, v23, v11
	v_log_f32_e32 v238, v17
	s_nop 0
	v_add_f32_e32 v187, v187, v238
	v_sub_f32_e32 v240, 0, v187
	v_sub_f32_e32 v241, 0, v187
	v_sub_f32_e32 v242, 0, v187
	v_sub_f32_e32 v243, 0, v187
	v_sub_f32_e32 v244, 0, v187
	v_sub_f32_e32 v245, 0, v187
	v_sub_f32_e32 v246, 0, v187
	v_sub_f32_e32 v247, 0, v187
	v_sub_f32_e32 v248, 0, v187
	v_sub_f32_e32 v249, 0, v187
	v_sub_f32_e32 v250, 0, v187
	v_sub_f32_e32 v251, 0, v187
	v_sub_f32_e32 v252, 0, v187
	v_sub_f32_e32 v253, 0, v187
	v_sub_f32_e32 v254, 0, v187
	v_sub_f32_e32 v255, 0, v187
	v_lshrrev_b32_e32 v22, 3, v98
	v_or3_b32 v2, s13, v183, v22
	v_lshlrev_b64 v[8:9], 13, v[2:3]
	v_lshl_add_u64 v[8:9], s[4:5], 0, v[8:9]
	v_lshlrev_b32_e32 v2, 2, v101
	v_lshl_add_u64 v[8:9], v[8:9], 0, v[2:3]
	v_and_b32_e32 v2, 0x70, v54
	v_lshl_add_u64 v[174:175], v[8:9], 0, v[2:3]
	ds_read_b128 v[8:11], v186 offset:64
	s_waitcnt lgkmcnt(2)
	v_mfma_f32_32x32x16_f16 v[66:81], v[18:21], v[118:121], v[66:81]
	v_div_scale_f32 v18, s[4:5], v16, v16, -v41
	v_rcp_f32_e32 v19, v18
	v_div_scale_f32 v20, vcc, -v41, v16, -v41
	s_mov_b32 s13, 0x20000
	v_mov_b32_e32 v24, v3
	s_waitcnt lgkmcnt(1)
	v_mfma_f32_32x32x16_f16 v[82:97], v[4:7], v[134:137], v[82:97]
	v_fma_f32 v4, -v18, v19, 1.0
	v_fmac_f32_e32 v19, v4, v19
	v_mul_f32_e32 v21, v20, v19
	ds_read_b128 v[4:7], v186 offset:9280
	ds_read_b128 v[12:15], v186 offset:96
	v_mov_b32_e32 v25, v3
	v_mov_b32_e32 v26, v3
	v_mov_b32_e32 v27, v3
	s_waitcnt lgkmcnt(2)
	v_mfma_f32_32x32x16_f16 v[66:81], v[8:11], v[122:125], v[66:81]
	v_fma_f32 v8, -v18, v21, v20
	v_fmac_f32_e32 v21, v8, v19
	v_fma_f32 v18, -v18, v21, v20
	v_div_scale_f32 v20, s[4:5], v17, v17, 1.0
	v_rcp_f32_e32 v23, v20
	ds_read_b128 v[8:11], v186 offset:9312
	s_waitcnt lgkmcnt(2)
	v_mfma_f32_32x32x16_f16 v[82:97], v[4:7], v[138:141], v[82:97]
	v_div_fmas_f32 v4, v18, v19, v21
	v_div_fixup_f32 v176, v4, v16, -v41
	v_fma_f32 v4, -v20, v23, 1.0
	v_fmac_f32_e32 v23, v4, v23
	v_div_scale_f32 v4, vcc, 1.0, v17, 1.0
	v_mul_f32_e32 v5, v4, v23
	v_fma_f32 v6, -v20, v5, v4
	v_fmac_f32_e32 v5, v6, v23
	s_waitcnt lgkmcnt(1)
	v_mfma_f32_32x32x16_f16 v[66:81], v[12:15], v[126:129], v[66:81]
	v_fma_f32 v4, -v20, v5, v4
	v_div_fmas_f32 v4, v4, v23, v5
	v_div_fixup_f32 v177, v4, v17, 1.0
	v_mul_u32_u24_e32 v4, 0x90, v22
	v_add3_u32 v189, v40, v4, v2
	v_mul_u32_u24_e32 v2, 0x90, v1
	v_lshlrev_b32_e32 v4, 2, v99
	s_waitcnt lgkmcnt(0)
	v_mfma_f32_32x32x16_f16 v[82:97], v[8:11], v[142:145], v[82:97]
	v_add3_u32 v190, v40, v2, v4
	v_mul_u32_u24_e32 v2, 0x48, v1
	v_lshl_add_u32 v2, v2, 1, 0
	v_lshlrev_b32_e32 v4, 1, v101
	v_add3_u32 v191, v2, v4, v100
	s_mov_b32 s4, 0x3f800000
	s_mov_b32 s5, 0x10000
	v_mov_b32_e32 v2, v3
	v_mov_b32_e32 v4, v3
	v_mov_b32_e32 v5, v3
	v_mov_b32_e32 v6, v3
	v_mov_b32_e32 v7, v3
	v_mov_b32_e32 v8, v3
	v_mov_b32_e32 v9, v3
	v_mov_b32_e32 v10, v3
	v_mov_b32_e32 v11, v3
	v_mov_b32_e32 v12, v3
	v_mov_b32_e32 v13, v3
	v_mov_b32_e32 v14, v3
	v_mov_b32_e32 v15, v3
	v_mov_b32_e32 v16, v3
	v_mov_b32_e32 v17, v3
	v_mov_b32_e32 v18, v3
	v_mov_b32_e32 v19, v3
	v_mov_b32_e32 v20, v3
	v_mov_b32_e32 v21, v3
	v_mov_b32_e32 v22, v3
	v_mov_b32_e32 v23, v3
	v_mov_b32_e32 v28, v3
	v_mov_b32_e32 v29, v3
	v_mov_b32_e32 v30, v3
	v_mov_b32_e32 v31, v3
	v_mov_b32_e32 v32, v3
	v_mov_b32_e32 v33, v3
	v_mov_b32_e32 v34, v3
	v_mov_b32_e32 v35, v3
	v_mov_b32_e32 v36, v3
	v_mov_b32_e32 v37, v3
	v_mov_b32_e32 v38, v3
	v_mov_b32_e32 v39, v3
	v_mov_b32_e32 v40, v3
	v_mov_b32_e32 v41, v3
	v_mov_b32_e32 v42, v3
	v_mov_b32_e32 v43, v3
	v_mov_b32_e32 v44, v3
	v_mov_b32_e32 v45, v3
	v_mov_b32_e32 v46, v3
	v_mov_b32_e32 v47, v3
	v_mov_b32_e32 v48, v3
	v_mov_b32_e32 v49, v3
	v_mov_b32_e32 v50, v3
	v_mov_b32_e32 v51, v3
	v_mov_b32_e32 v52, v3
	v_mov_b32_e32 v53, v3
	v_mov_b32_e32 v54, v3
	v_mov_b32_e32 v56, v3
	v_mov_b32_e32 v57, v3
	v_mov_b32_e32 v58, v3
	v_mov_b32_e32 v59, v3
	v_mov_b32_e32 v60, v3
	v_mov_b32_e32 v61, v3
	v_mov_b32_e32 v62, v3
	v_mov_b32_e32 v63, v3
	v_mov_b32_e32 v64, v3
	v_mov_b32_e32 v65, v3
	v_add_u32_e32 v192, 0xd800, v191
	v_sub_f32_e32 v66, v66, v187
	v_sub_f32_e32 v67, v67, v187
	v_sub_f32_e32 v68, v68, v187
	v_sub_f32_e32 v69, v69, v187
	v_sub_f32_e32 v70, v70, v187
	v_sub_f32_e32 v71, v71, v187
	v_sub_f32_e32 v72, v72, v187
	v_sub_f32_e32 v73, v73, v187
	v_sub_f32_e32 v74, v74, v187
	v_sub_f32_e32 v75, v75, v187
	v_sub_f32_e32 v76, v76, v187
	v_sub_f32_e32 v77, v77, v187
	v_sub_f32_e32 v78, v78, v187
	v_sub_f32_e32 v79, v79, v187
	v_sub_f32_e32 v80, v80, v187
	v_sub_f32_e32 v81, v81, v187
	s_mov_b32 s27, 0x42c80000
	v_cmp_gt_f32_e64 vcc, |v188|, s27
	s_cbranch_vccnz .Ll2_gen
	v_sub_f32_e32 v238, 0, v188
	v_exp_f32_e32 v238, v238
	s_nop 0
	v_mul_f32_e32 v176, v176, v238
	s_barrier
	s_branch .Ll2f_top
